# iteration kernels: each wave pre-touches one far branch target of the block switch (instruction-cache line) while the slot loads are in flight
# speedup vs baseline: 1.0197x; 1.0197x over previous
_Z6k_iterILb0ELb0EEvPKfS1_PKiPK15HIP_vector_typeIfLj4EES7_S1_S1_S3_S1_PfS8_S1_S3_PDF16_PS5_SA_PiSA_SB_:
	s_and_b32 s38, s0, 0xfffff000
	s_mov_b32 s39, s1
	s_load_dwordx2 s[8:9], s[0:1], 0x80
	s_load_dwordx4 s[4:7], s[0:1], 0x70
	s_load_dwordx4 s[16:19], s[0:1], 0x40
	s_load_dwordx2 s[40:41], s[0:1], 0x90
	s_load_dwordx2 s[42:43], s[0:1], 0x88
	v_readfirstlane_b32 s12, v0
	v_cmp_gt_u32_e64 s[14:15], 64, v0
	v_lshlrev_b32_e32 v1, 2, v0
	s_and_saveexec_b64 s[10:11], s[14:15]
	v_mov_b32_e32 v2, 0
	ds_write_b32 v1, v2 offset:5152
	s_or_b64 exec, exec, s[10:11]
	s_lshl_b32 s3, s2, 5
	s_and_b32 s3, s3, 0xe0
	s_lshr_b32 s2, s2, 3
	s_add_i32 s2, s3, s2
	s_lshl_b32 s25, s2, 6
	v_and_b32_e32 v2, 31, v0
	v_or_b32_e32 v4, s25, v2
	v_mov_b32_e32 v5, 0
	s_lshr_b32 s27, s12, 6
	s_lshl_b32 s32, s27, 2
	s_lshr_b32 s32, 0x73261540, s32
	s_lshl_b32 s32, s32, 5
	s_and_b32 s32, s32, 0xe0
	v_or_b32_e32 v176, s32, v2
	v_lshlrev_b32_e32 v177, 4, v176
	v_add_u32_e32 v178, 0x1000, v177
	v_add_u32_e32 v179, 0x2000, v177
	v_add_u32_e32 v180, 0x3000, v177
	v_add_u32_e32 v181, 0x4000, v177
	v_add_u32_e32 v182, 0x5000, v177
	s_mov_b32 s3, 0
	s_lshl_b64 s[34:35], s[2:3], 16
	s_lshl_b32 s33, s2, 2
	s_waitcnt lgkmcnt(0)
	s_load_dword s24, s[8:9], s33 offset:0x0
	s_load_dword s41, s[40:41], s33 offset:0x0
	s_add_u32 s20, s4, s34
	s_addc_u32 s21, s5, s35
	v_lshl_add_u64 v[4:5], v[4:5], 4, s[6:7]
	global_load_dwordx3 v[30:32], v[4:5], off
	global_load_dwordx3 v[26:28], v[4:5], off offset:512
	global_load_dwordx4 v[2:5], v177, s[20:21]
	global_load_dwordx4 v[6:9], v178, s[20:21]
	global_load_dwordx4 v[10:13], v179, s[20:21]
	global_load_dwordx4 v[14:17], v180, s[20:21]
	global_load_dwordx4 v[18:21], v181, s[20:21]
	global_load_dwordx4 v[22:25], v182, s[20:21]
	s_cmp_eq_u32 s27, 0
	s_cbranch_scc1 .Lffc_touch_14
	s_cmp_eq_u32 s27, 1
	s_cbranch_scc1 .Lffc_touch_19
	s_cmp_eq_u32 s27, 2
	s_cbranch_scc1 .Lffc_touch_11
	s_cmp_eq_u32 s27, 3
	s_cbranch_scc1 .Lffc_touch_15
	s_cmp_eq_u32 s27, 4
	s_cbranch_scc1 .Lffc_touch_31
	s_cmp_eq_u32 s27, 5
	s_cbranch_scc1 .Lffc_touch_37
	s_cmp_eq_u32 s27, 6
	s_cbranch_scc1 .Lffc_touch_39
.Lffc_touch_ret:
	v_and_b32_e32 v38, 63, v0
	v_mov_b32_e32 v29, 0xff800000
	v_cmp_gt_u32_e64 s[0:1], 32, v38
	s_waitcnt lgkmcnt(0)
	s_cmpk_gt_i32 s24, 0x600
	s_cselect_b64 s[22:23], -1, 0
	s_cmpk_lt_i32 s24, 0x601
	s_cbranch_scc1 .LBB3_6
	s_and_saveexec_b64 s[8:9], s[14:15]
	s_cbranch_execz .LBB3_5
	v_or_b32_e32 v178, s25, v0
	v_mov_b32_e32 v179, 0
	v_lshl_add_u64 v[178:179], v[178:179], 4, s[6:7]
	global_load_dwordx4 v[178:181], v[178:179], off
	v_lshlrev_b32_e32 v177, 4, v0
	s_waitcnt vmcnt(0)
	ds_write_b128 v177, v[178:181] offset:2080

.Lffc_nocache1:
	s_cmp_lt_i32 s26, 4
	global_load_dword v133, v[6:7], off
	global_load_dword v132, v[8:9], off
	global_load_dword v131, v[10:11], off
	global_load_dword v130, v[12:13], off
	global_load_dword v129, v[14:15], off
	global_load_dword v128, v[4:5], off
	v_max_f32_e32 v6, v32, v32
	v_cndmask_b32_e64 v4, v31, v30, s[0:1]
	v_max_f32_e32 v6, 0xc6ea6000, v6
	v_cndmask_b32_e64 v6, v6, 1.0, s[0:1]
	v_and_b32_e32 v7, 0xffff0000, v4
	v_sub_f32_e32 v8, v4, v7
	v_or_b32_sdwa v22, v4, v7 dst_sel:DWORD dst_unused:UNUSED_PAD src0_sel:WORD_1 src1_sel:DWORD
	v_and_b32_e32 v4, 0xffff0000, v6
	v_sub_f32_e32 v7, v6, v4
	v_or_b32_sdwa v24, v6, v4 dst_sel:DWORD dst_unused:UNUSED_PAD src0_sel:WORD_1 src1_sel:DWORD
	v_or_b32_sdwa v23, v8, v4 dst_sel:DWORD dst_unused:UNUSED_PAD src0_sel:WORD_1 src1_sel:DWORD
	v_max_f32_e32 v4, v28, v28
	v_cndmask_b32_e64 v5, v27, v26, s[0:1]
	v_and_b32_e32 v9, 0xffff0000, v7
	v_max_f32_e32 v4, 0xc6ea6000, v4
	v_sub_f32_e32 v9, v7, v9
	v_lshrrev_b32_e32 v7, 16, v7
	v_cndmask_b32_e64 v4, v4, 1.0, s[0:1]
	v_and_b32_e32 v6, 0xffff0000, v5
	v_and_or_b32 v25, v9, s2, v7
	v_sub_f32_e32 v7, v5, v6
	v_or_b32_sdwa v18, v5, v6 dst_sel:DWORD dst_unused:UNUSED_PAD src0_sel:WORD_1 src1_sel:DWORD
	v_and_b32_e32 v5, 0xffff0000, v4
	v_sub_f32_e32 v6, v4, v5
	v_and_b32_e32 v8, 0xffff0000, v6
	v_sub_f32_e32 v8, v6, v8
	v_lshrrev_b32_e32 v6, 16, v6
	v_or_b32_sdwa v20, v4, v5 dst_sel:DWORD dst_unused:UNUSED_PAD src0_sel:WORD_1 src1_sel:DWORD
	v_or_b32_sdwa v19, v7, v5 dst_sel:DWORD dst_unused:UNUSED_PAD src0_sel:WORD_1 src1_sel:DWORD
	v_and_or_b32 v21, v8, s2, v6
	s_mov_b64 s[2:3], 0
	s_cbranch_scc1 .LBB3_11
	s_cmp_gt_i32 s26, 4
	s_cbranch_scc0 .LBB3_14
	s_cmp_gt_i32 s26, 5
	s_cbranch_scc0 .LBB3_15
	s_cmp_eq_u32 s26, 6
	s_mov_b64 s[4:5], 0
	s_cbranch_scc0 .LBB3_48
	v_and_b32_e32 v4, 0xffff0000, v2
	v_max_f32_e32 v3, v3, v3
	v_sub_f32_e32 v4, v2, v4
	v_max_f32_e32 v3, 0xc6ea6000, v3
	v_and_b32_e32 v5, 0xffff0000, v3
	v_and_b32_e32 v4, 0xffff0000, v4
	v_or_b32_sdwa v75, v5, v2 dst_sel:DWORD dst_unused:UNUSED_PAD src0_sel:DWORD src1_sel:WORD_1
	v_or_b32_sdwa v74, v4, v2 dst_sel:DWORD dst_unused:UNUSED_PAD src0_sel:DWORD src1_sel:WORD_1
	v_sub_f32_e32 v2, v3, v5
	v_and_b32_e32 v4, 0xffff0000, v2
	s_mov_b32 s6, 0xffff0000
	v_sub_f32_e32 v4, v2, v4
	v_lshrrev_b32_e32 v2, 16, v2
	v_and_or_b32 v76, v4, s6, v2
	v_or_b32_sdwa v77, v3, v5 dst_sel:DWORD dst_unused:UNUSED_PAD src0_sel:WORD_1 src1_sel:DWORD
	s_movk_i32 s6, 0xfc00
	s_mov_b64 s[8:9], -1
	v_mfma_f32_32x32x16_bf16 v[2:17], v[22:25], v[74:77], 0
	s_nop 11
	v_cvt_pk_f16_f32 v2, v2, v3
	v_cvt_pk_f16_f32 v3, v4, v5
	v_pk_max_i16 v2, v2, s6 op_sel_hi:[1,0]
	v_pk_max_i16 v3, v3, s6 op_sel_hi:[1,0]
	s_nop 0
	v_exp_f16_e32 v43, v2
	v_exp_f16_e32 v45, v3
	v_exp_f16_sdwa v43, v2 dst_sel:WORD_1 dst_unused:UNUSED_PRESERVE src0_sel:WORD_1
	v_exp_f16_sdwa v45, v3 dst_sel:WORD_1 dst_unused:UNUSED_PRESERVE src0_sel:WORD_1
	v_cvt_pk_f16_f32 v2, v6, v7
	v_cvt_pk_f16_f32 v3, v8, v9
	v_pk_max_i16 v2, v2, s6 op_sel_hi:[1,0]
	v_pk_max_i16 v3, v3, s6 op_sel_hi:[1,0]
	s_nop 0
	v_exp_f16_e32 v50, v2
	v_exp_f16_e32 v54, v3
	v_exp_f16_sdwa v50, v2 dst_sel:WORD_1 dst_unused:UNUSED_PRESERVE src0_sel:WORD_1
	v_exp_f16_sdwa v54, v3 dst_sel:WORD_1 dst_unused:UNUSED_PRESERVE src0_sel:WORD_1
	v_cvt_pk_f16_f32 v2, v10, v11
	v_cvt_pk_f16_f32 v3, v12, v13
	v_pk_max_i16 v2, v2, s6 op_sel_hi:[1,0]
	v_pk_max_i16 v3, v3, s6 op_sel_hi:[1,0]
	s_nop 0
	v_exp_f16_e32 v58, v2
	v_exp_f16_e32 v61, v3
	v_exp_f16_sdwa v58, v2 dst_sel:WORD_1 dst_unused:UNUSED_PRESERVE src0_sel:WORD_1
	v_exp_f16_sdwa v61, v3 dst_sel:WORD_1 dst_unused:UNUSED_PRESERVE src0_sel:WORD_1
	v_cvt_pk_f16_f32 v2, v14, v15
	v_cvt_pk_f16_f32 v3, v16, v17
	v_pk_max_i16 v2, v2, s6 op_sel_hi:[1,0]
	v_pk_max_i16 v3, v3, s6 op_sel_hi:[1,0]
	s_nop 0
	v_exp_f16_e32 v64, v2
	v_exp_f16_e32 v66, v3
	v_exp_f16_sdwa v64, v2 dst_sel:WORD_1 dst_unused:UNUSED_PRESERVE src0_sel:WORD_1
	v_exp_f16_sdwa v66, v3 dst_sel:WORD_1 dst_unused:UNUSED_PRESERVE src0_sel:WORD_1
	v_mfma_f32_32x32x16_bf16 v[2:17], v[18:21], v[74:77], 0
	s_nop 11
	v_cvt_pk_f16_f32 v2, v2, v3
	v_cvt_pk_f16_f32 v3, v4, v5
	v_pk_max_i16 v2, v2, s6 op_sel_hi:[1,0]
	v_pk_max_i16 v3, v3, s6 op_sel_hi:[1,0]
	s_nop 0
	v_exp_f16_e32 v72, v2
	v_exp_f16_e32 v76, v3
	v_exp_f16_sdwa v72, v2 dst_sel:WORD_1 dst_unused:UNUSED_PRESERVE src0_sel:WORD_1
	v_exp_f16_sdwa v76, v3 dst_sel:WORD_1 dst_unused:UNUSED_PRESERVE src0_sel:WORD_1
	v_cvt_pk_f16_f32 v2, v6, v7
	v_cvt_pk_f16_f32 v3, v8, v9
	v_pk_max_i16 v2, v2, s6 op_sel_hi:[1,0]
	v_pk_max_i16 v3, v3, s6 op_sel_hi:[1,0]
	s_nop 0
	v_exp_f16_e32 v83, v2
	v_exp_f16_e32 v85, v3
	v_exp_f16_sdwa v83, v2 dst_sel:WORD_1 dst_unused:UNUSED_PRESERVE src0_sel:WORD_1
	v_exp_f16_sdwa v85, v3 dst_sel:WORD_1 dst_unused:UNUSED_PRESERVE src0_sel:WORD_1
	v_cvt_pk_f16_f32 v2, v10, v11
	v_cvt_pk_f16_f32 v3, v12, v13
	v_pk_max_i16 v2, v2, s6 op_sel_hi:[1,0]
	v_pk_max_i16 v3, v3, s6 op_sel_hi:[1,0]
	s_nop 0
	v_exp_f16_e32 v89, v2
	v_exp_f16_e32 v92, v3
	v_exp_f16_sdwa v89, v2 dst_sel:WORD_1 dst_unused:UNUSED_PRESERVE src0_sel:WORD_1
	v_exp_f16_sdwa v92, v3 dst_sel:WORD_1 dst_unused:UNUSED_PRESERVE src0_sel:WORD_1
	v_cvt_pk_f16_f32 v2, v14, v15
	v_cvt_pk_f16_f32 v3, v16, v17
	v_pk_max_i16 v2, v2, s6 op_sel_hi:[1,0]
	v_pk_max_i16 v3, v3, s6 op_sel_hi:[1,0]
	s_nop 0
	v_exp_f16_e32 v95, v2
	v_exp_f16_e32 v96, v3
	v_exp_f16_sdwa v95, v2 dst_sel:WORD_1 dst_unused:UNUSED_PRESERVE src0_sel:WORD_1
	v_exp_f16_sdwa v96, v3 dst_sel:WORD_1 dst_unused:UNUSED_PRESERVE src0_sel:WORD_1
	s_and_b64 vcc, exec, s[4:5]
	s_cbranch_vccnz .LBB3_16
	s_branch .LBB3_17
.Lffc_touch_11:
	s_branch .Lffc_touch_ret
.LBB3_11:
	s_mov_b64 s[4:5], 0
	s_cbranch_execnz .LBB3_24

.LBB3_13:
	v_max_f32_e32 v2, v70, v70
	v_max_f32_e32 v2, 0xc6ea6000, v2
	v_and_b32_e32 v4, 0xffff0000, v2
	v_and_b32_e32 v3, 0xffff0000, v68
	v_sub_f32_e32 v5, v2, v4
	v_sub_f32_e32 v3, v68, v3
	v_and_b32_e32 v6, 0xffff0000, v5
	s_mov_b32 s4, 0xffff0000
	v_and_b32_e32 v3, 0xffff0000, v3
	v_sub_f32_e32 v6, v5, v6
	v_lshrrev_b32_e32 v5, 16, v5
	v_or_b32_sdwa v101, v4, v68 dst_sel:DWORD dst_unused:UNUSED_PAD src0_sel:DWORD src1_sel:WORD_1
	v_or_b32_sdwa v100, v3, v68 dst_sel:DWORD dst_unused:UNUSED_PAD src0_sel:DWORD src1_sel:WORD_1
	v_and_or_b32 v102, v6, s4, v5
	v_or_b32_sdwa v103, v2, v4 dst_sel:DWORD dst_unused:UNUSED_PAD src0_sel:WORD_1 src1_sel:DWORD
	s_movk_i32 s4, 0xfc00
	s_nop 0
	v_mfma_f32_32x32x16_bf16 v[2:17], v[22:25], v[100:103], 0
	s_nop 11
	v_cvt_pk_f16_f32 v2, v2, v3
	v_cvt_pk_f16_f32 v3, v4, v5
	v_pk_max_i16 v2, v2, s4 op_sel_hi:[1,0]
	v_pk_max_i16 v3, v3, s4 op_sel_hi:[1,0]
	s_nop 0
	v_exp_f16_e32 v68, v2
	v_exp_f16_e32 v70, v3
	v_exp_f16_sdwa v68, v2 dst_sel:WORD_1 dst_unused:UNUSED_PRESERVE src0_sel:WORD_1
	v_exp_f16_sdwa v70, v3 dst_sel:WORD_1 dst_unused:UNUSED_PRESERVE src0_sel:WORD_1
	v_cvt_pk_f16_f32 v2, v6, v7
	v_cvt_pk_f16_f32 v3, v8, v9
	v_pk_max_i16 v2, v2, s4 op_sel_hi:[1,0]
	v_pk_max_i16 v3, v3, s4 op_sel_hi:[1,0]
	s_nop 0
	v_exp_f16_e32 v71, v2
	v_exp_f16_e32 v73, v3
	v_exp_f16_sdwa v71, v2 dst_sel:WORD_1 dst_unused:UNUSED_PRESERVE src0_sel:WORD_1
	v_exp_f16_sdwa v73, v3 dst_sel:WORD_1 dst_unused:UNUSED_PRESERVE src0_sel:WORD_1
	v_cvt_pk_f16_f32 v2, v10, v11
	v_cvt_pk_f16_f32 v3, v12, v13
	v_pk_max_i16 v2, v2, s4 op_sel_hi:[1,0]
	v_pk_max_i16 v3, v3, s4 op_sel_hi:[1,0]
	s_nop 0
	v_exp_f16_e32 v77, v2
	v_exp_f16_e32 v78, v3
	v_exp_f16_sdwa v77, v2 dst_sel:WORD_1 dst_unused:UNUSED_PRESERVE src0_sel:WORD_1
	v_exp_f16_sdwa v78, v3 dst_sel:WORD_1 dst_unused:UNUSED_PRESERVE src0_sel:WORD_1
	v_cvt_pk_f16_f32 v2, v14, v15
	v_cvt_pk_f16_f32 v3, v16, v17
	v_pk_max_i16 v2, v2, s4 op_sel_hi:[1,0]
	v_pk_max_i16 v3, v3, s4 op_sel_hi:[1,0]
	s_nop 0
	v_exp_f16_e32 v81, v2
	v_exp_f16_e32 v82, v3
	v_exp_f16_sdwa v81, v2 dst_sel:WORD_1 dst_unused:UNUSED_PRESERVE src0_sel:WORD_1
	v_exp_f16_sdwa v82, v3 dst_sel:WORD_1 dst_unused:UNUSED_PRESERVE src0_sel:WORD_1
	v_mfma_f32_32x32x16_bf16 v[2:17], v[18:21], v[100:103], 0
	s_nop 11
	v_cvt_pk_f16_f32 v2, v2, v3
	v_cvt_pk_f16_f32 v3, v4, v5
	v_pk_max_i16 v2, v2, s4 op_sel_hi:[1,0]
	v_pk_max_i16 v3, v3, s4 op_sel_hi:[1,0]
	s_nop 0
	v_exp_f16_e32 v84, v2
	v_exp_f16_e32 v86, v3
	v_exp_f16_sdwa v84, v2 dst_sel:WORD_1 dst_unused:UNUSED_PRESERVE src0_sel:WORD_1
	v_exp_f16_sdwa v86, v3 dst_sel:WORD_1 dst_unused:UNUSED_PRESERVE src0_sel:WORD_1
	v_cvt_pk_f16_f32 v2, v6, v7
	v_cvt_pk_f16_f32 v3, v8, v9
	v_pk_max_i16 v2, v2, s4 op_sel_hi:[1,0]
	v_pk_max_i16 v3, v3, s4 op_sel_hi:[1,0]
	s_nop 0
	v_exp_f16_e32 v87, v2
	v_exp_f16_e32 v88, v3
	v_exp_f16_sdwa v87, v2 dst_sel:WORD_1 dst_unused:UNUSED_PRESERVE src0_sel:WORD_1
	v_exp_f16_sdwa v88, v3 dst_sel:WORD_1 dst_unused:UNUSED_PRESERVE src0_sel:WORD_1
	v_cvt_pk_f16_f32 v2, v10, v11
	v_cvt_pk_f16_f32 v3, v12, v13
	v_pk_max_i16 v2, v2, s4 op_sel_hi:[1,0]
	v_pk_max_i16 v3, v3, s4 op_sel_hi:[1,0]
	s_nop 0
	v_exp_f16_e32 v90, v2
	v_exp_f16_e32 v91, v3
	v_exp_f16_sdwa v90, v2 dst_sel:WORD_1 dst_unused:UNUSED_PRESERVE src0_sel:WORD_1
	v_exp_f16_sdwa v91, v3 dst_sel:WORD_1 dst_unused:UNUSED_PRESERVE src0_sel:WORD_1
	v_cvt_pk_f16_f32 v2, v14, v15
	v_cvt_pk_f16_f32 v3, v16, v17
	v_pk_max_i16 v2, v2, s4 op_sel_hi:[1,0]
	v_pk_max_i16 v3, v3, s4 op_sel_hi:[1,0]
	s_mov_b64 s[4:5], -1
	v_exp_f16_e32 v93, v2
	v_exp_f16_e32 v94, v3
	v_exp_f16_sdwa v93, v2 dst_sel:WORD_1 dst_unused:UNUSED_PRESERVE src0_sel:WORD_1
	v_exp_f16_sdwa v94, v3 dst_sel:WORD_1 dst_unused:UNUSED_PRESERVE src0_sel:WORD_1
	s_andn2_b64 vcc, exec, s[6:7]
	s_cbranch_vccz .LBB3_30
	s_branch .LBB3_31
.Lffc_touch_14:
	s_branch .Lffc_touch_ret
.LBB3_14:
	s_mov_b64 s[4:5], 0
	s_cbranch_execz .LBB3_21
	s_branch .LBB3_20
.Lffc_touch_15:
	s_branch .Lffc_touch_ret
.LBB3_15:
	s_mov_b64 s[8:9], 0
	s_cbranch_execz .LBB3_17

.LBB3_17:
	s_mov_b64 s[6:7], 0
	s_andn2_b64 vcc, exec, s[8:9]
	s_mov_b64 s[4:5], 0
	s_cbranch_vccnz .LBB3_19
	v_max_f32_e32 v2, v48, v48
	v_max_f32_e32 v2, 0xc6ea6000, v2
	v_and_b32_e32 v4, 0xffff0000, v2
	v_and_b32_e32 v3, 0xffff0000, v46
	v_sub_f32_e32 v5, v2, v4
	v_sub_f32_e32 v3, v46, v3
	v_and_b32_e32 v6, 0xffff0000, v5
	s_mov_b32 s4, 0xffff0000
	v_and_b32_e32 v3, 0xffff0000, v3
	v_sub_f32_e32 v6, v5, v6
	v_lshrrev_b32_e32 v5, 16, v5
	v_or_b32_sdwa v47, v4, v46 dst_sel:DWORD dst_unused:UNUSED_PAD src0_sel:DWORD src1_sel:WORD_1
	v_or_b32_sdwa v46, v3, v46 dst_sel:DWORD dst_unused:UNUSED_PAD src0_sel:DWORD src1_sel:WORD_1
	v_and_or_b32 v48, v6, s4, v5
	v_or_b32_sdwa v49, v2, v4 dst_sel:DWORD dst_unused:UNUSED_PAD src0_sel:WORD_1 src1_sel:DWORD
	s_movk_i32 s4, 0xfc00
	s_nop 0
	v_mfma_f32_32x32x16_bf16 v[2:17], v[22:25], v[46:49], 0
	s_nop 11
	v_cvt_pk_f16_f32 v2, v2, v3
	v_cvt_pk_f16_f32 v3, v4, v5
	v_pk_max_i16 v2, v2, s4 op_sel_hi:[1,0]
	v_pk_max_i16 v3, v3, s4 op_sel_hi:[1,0]
	s_nop 0
	v_exp_f16_e32 v26, v2
	v_exp_f16_e32 v27, v3
	v_exp_f16_sdwa v26, v2 dst_sel:WORD_1 dst_unused:UNUSED_PRESERVE src0_sel:WORD_1
	v_exp_f16_sdwa v27, v3 dst_sel:WORD_1 dst_unused:UNUSED_PRESERVE src0_sel:WORD_1
	v_cvt_pk_f16_f32 v2, v6, v7
	v_cvt_pk_f16_f32 v3, v8, v9
	v_pk_max_i16 v2, v2, s4 op_sel_hi:[1,0]
	v_pk_max_i16 v3, v3, s4 op_sel_hi:[1,0]
	s_nop 0
	v_exp_f16_e32 v28, v2
	v_exp_f16_e32 v30, v3
	v_exp_f16_sdwa v28, v2 dst_sel:WORD_1 dst_unused:UNUSED_PRESERVE src0_sel:WORD_1
	v_exp_f16_sdwa v30, v3 dst_sel:WORD_1 dst_unused:UNUSED_PRESERVE src0_sel:WORD_1
	v_cvt_pk_f16_f32 v2, v10, v11
	v_cvt_pk_f16_f32 v3, v12, v13
	v_pk_max_i16 v2, v2, s4 op_sel_hi:[1,0]
	v_pk_max_i16 v3, v3, s4 op_sel_hi:[1,0]
	s_nop 0
	v_exp_f16_e32 v31, v2
	v_exp_f16_e32 v32, v3
	v_exp_f16_sdwa v31, v2 dst_sel:WORD_1 dst_unused:UNUSED_PRESERVE src0_sel:WORD_1
	v_exp_f16_sdwa v32, v3 dst_sel:WORD_1 dst_unused:UNUSED_PRESERVE src0_sel:WORD_1
	v_cvt_pk_f16_f32 v2, v14, v15
	v_cvt_pk_f16_f32 v3, v16, v17
	v_pk_max_i16 v2, v2, s4 op_sel_hi:[1,0]
	v_pk_max_i16 v3, v3, s4 op_sel_hi:[1,0]
	s_nop 0
	v_exp_f16_e32 v39, v2
	v_exp_f16_e32 v40, v3
	v_exp_f16_sdwa v39, v2 dst_sel:WORD_1 dst_unused:UNUSED_PRESERVE src0_sel:WORD_1
	v_exp_f16_sdwa v40, v3 dst_sel:WORD_1 dst_unused:UNUSED_PRESERVE src0_sel:WORD_1
	v_mfma_f32_32x32x16_bf16 v[2:17], v[18:21], v[46:49], 0
	s_nop 11
	v_cvt_pk_f16_f32 v2, v2, v3
	v_cvt_pk_f16_f32 v3, v4, v5
	v_pk_max_i16 v2, v2, s4 op_sel_hi:[1,0]
	v_pk_max_i16 v3, v3, s4 op_sel_hi:[1,0]
	s_nop 0
	v_exp_f16_e32 v41, v2
	v_exp_f16_e32 v42, v3
	v_exp_f16_sdwa v41, v2 dst_sel:WORD_1 dst_unused:UNUSED_PRESERVE src0_sel:WORD_1
	v_exp_f16_sdwa v42, v3 dst_sel:WORD_1 dst_unused:UNUSED_PRESERVE src0_sel:WORD_1
	v_cvt_pk_f16_f32 v2, v6, v7
	v_cvt_pk_f16_f32 v3, v8, v9
	v_pk_max_i16 v2, v2, s4 op_sel_hi:[1,0]
	v_pk_max_i16 v3, v3, s4 op_sel_hi:[1,0]
	s_nop 0
	v_exp_f16_e32 v44, v2
	v_exp_f16_e32 v47, v3
	v_exp_f16_sdwa v44, v2 dst_sel:WORD_1 dst_unused:UNUSED_PRESERVE src0_sel:WORD_1
	v_exp_f16_sdwa v47, v3 dst_sel:WORD_1 dst_unused:UNUSED_PRESERVE src0_sel:WORD_1
	v_cvt_pk_f16_f32 v2, v10, v11
	v_cvt_pk_f16_f32 v3, v12, v13
	v_pk_max_i16 v2, v2, s4 op_sel_hi:[1,0]
	v_pk_max_i16 v3, v3, s4 op_sel_hi:[1,0]
	s_nop 0
	v_exp_f16_e32 v51, v2
	v_exp_f16_e32 v53, v3
	v_exp_f16_sdwa v51, v2 dst_sel:WORD_1 dst_unused:UNUSED_PRESERVE src0_sel:WORD_1
	v_exp_f16_sdwa v53, v3 dst_sel:WORD_1 dst_unused:UNUSED_PRESERVE src0_sel:WORD_1
	v_cvt_pk_f16_f32 v2, v14, v15
	v_cvt_pk_f16_f32 v3, v16, v17
	v_pk_max_i16 v2, v2, s4 op_sel_hi:[1,0]
	v_pk_max_i16 v3, v3, s4 op_sel_hi:[1,0]
	s_mov_b64 s[4:5], -1
	v_exp_f16_e32 v57, v2
	v_exp_f16_e32 v59, v3
	v_exp_f16_sdwa v57, v2 dst_sel:WORD_1 dst_unused:UNUSED_PRESERVE src0_sel:WORD_1
	v_exp_f16_sdwa v59, v3 dst_sel:WORD_1 dst_unused:UNUSED_PRESERVE src0_sel:WORD_1
	s_and_b64 vcc, exec, s[6:7]
	s_cbranch_vccz .LBB3_21
	s_branch .LBB3_20
.Lffc_touch_19:
	s_branch .Lffc_touch_ret
.LBB3_19:
	s_and_b64 vcc, exec, s[6:7]
	s_cbranch_vccz .LBB3_21

.LBB3_29:
	s_mov_b64 s[4:5], 0
	s_andn2_b64 vcc, exec, s[6:7]
	s_cbranch_vccnz .LBB3_31
.LBB3_30:
	s_mov_b64 s[4:5], -1
	s_branch .LBB3_31
.Lffc_touch_31:
	s_branch .Lffc_touch_ret
.LBB3_31:
	s_andn2_b64 vcc, exec, s[4:5]
	s_cbranch_vccnz .LBB3_33
	s_cmp_eq_u32 s36, 0
	s_cbranch_scc1 .Lffc_nb1_compute
	s_waitcnt vmcnt(6)
	v_mov_b32_e32 v98, v200
	v_mov_b32_e32 v97, v201
	v_mov_b32_e32 v100, v202
	v_mov_b32_e32 v99, v203
	v_mov_b32_e32 v102, v204
	v_mov_b32_e32 v101, v205
	v_mov_b32_e32 v104, v206
	v_mov_b32_e32 v103, v207
	v_mov_b32_e32 v106, v208
	v_mov_b32_e32 v105, v209
	v_mov_b32_e32 v108, v210
	v_mov_b32_e32 v107, v211
	v_mov_b32_e32 v110, v212
	v_mov_b32_e32 v109, v213
	v_mov_b32_e32 v112, v214
	v_mov_b32_e32 v111, v215
	s_mov_b64 s[4:5], -1
	s_andn2_b64 vcc, exec, s[2:3]
	s_cbranch_vccz .LBB3_34
	s_branch .LBB3_37

.LBB3_34:
	s_cmp_eq_u32 s26, 1
	s_cbranch_scc0 .LBB3_36
	s_mov_b64 s[4:5], -1
.LBB3_36:
	s_branch .LBB3_37
.Lffc_touch_37:
	s_branch .Lffc_touch_ret
.LBB3_37:
	s_and_b64 vcc, exec, s[4:5]
	s_cbranch_vccz .LBB3_39
	s_cmp_eq_u32 s47, 0
	s_cbranch_scc1 .Lffc_nb0_compute
	s_waitcnt vmcnt(6)
	v_mov_b32_e32 v117, v184
	v_mov_b32_e32 v113, v185
	v_mov_b32_e32 v118, v186
	v_mov_b32_e32 v114, v187
	v_mov_b32_e32 v120, v188
	v_mov_b32_e32 v115, v189
	v_mov_b32_e32 v122, v190
	v_mov_b32_e32 v116, v191
	v_mov_b32_e32 v124, v192
	v_mov_b32_e32 v119, v193
	v_mov_b32_e32 v125, v194
	v_mov_b32_e32 v121, v195
	v_mov_b32_e32 v126, v196
	v_mov_b32_e32 v123, v197
	v_mov_b32_e32 v127, v198
	v_mov_b32_e32 v17, v199
	s_branch .LBB3_39
.Lffc_nb0_compute:
	v_max_f32_e32 v2, v135, v135
	v_max_f32_e32 v2, 0xc6ea6000, v2
	v_and_b32_e32 v4, 0xffff0000, v2
	v_and_b32_e32 v3, 0xffff0000, v134
	v_sub_f32_e32 v5, v2, v4
	v_sub_f32_e32 v3, v134, v3
	v_and_b32_e32 v6, 0xffff0000, v5
	s_mov_b32 s2, 0xffff0000
	v_and_b32_e32 v3, 0xffff0000, v3
	v_sub_f32_e32 v6, v5, v6
	v_lshrrev_b32_e32 v5, 16, v5
	v_or_b32_sdwa v125, v4, v134 dst_sel:DWORD dst_unused:UNUSED_PAD src0_sel:DWORD src1_sel:WORD_1
	v_or_b32_sdwa v124, v3, v134 dst_sel:DWORD dst_unused:UNUSED_PAD src0_sel:DWORD src1_sel:WORD_1
	v_and_or_b32 v126, v6, s2, v5
	v_or_b32_sdwa v127, v2, v4 dst_sel:DWORD dst_unused:UNUSED_PAD src0_sel:WORD_1 src1_sel:DWORD
	s_movk_i32 s2, 0xfc00
	s_nop 0
	v_mfma_f32_32x32x16_bf16 v[2:17], v[22:25], v[124:127], 0
	s_nop 11
	v_cvt_pk_f16_f32 v2, v2, v3
	v_cvt_pk_f16_f32 v3, v4, v5
	v_pk_max_i16 v2, v2, s2 op_sel_hi:[1,0]
	v_pk_max_i16 v3, v3, s2 op_sel_hi:[1,0]
	s_nop 0
	v_exp_f16_e32 v117, v2
	v_exp_f16_e32 v113, v3
	v_exp_f16_sdwa v117, v2 dst_sel:WORD_1 dst_unused:UNUSED_PRESERVE src0_sel:WORD_1
	v_exp_f16_sdwa v113, v3 dst_sel:WORD_1 dst_unused:UNUSED_PRESERVE src0_sel:WORD_1
	v_cvt_pk_f16_f32 v2, v6, v7
	v_cvt_pk_f16_f32 v3, v8, v9
	v_pk_max_i16 v2, v2, s2 op_sel_hi:[1,0]
	v_pk_max_i16 v3, v3, s2 op_sel_hi:[1,0]
	s_nop 0
	v_exp_f16_e32 v118, v2
	v_exp_f16_e32 v114, v3
	v_exp_f16_sdwa v118, v2 dst_sel:WORD_1 dst_unused:UNUSED_PRESERVE src0_sel:WORD_1
	v_exp_f16_sdwa v114, v3 dst_sel:WORD_1 dst_unused:UNUSED_PRESERVE src0_sel:WORD_1
	v_cvt_pk_f16_f32 v2, v10, v11
	v_cvt_pk_f16_f32 v3, v12, v13
	v_pk_max_i16 v2, v2, s2 op_sel_hi:[1,0]
	v_pk_max_i16 v3, v3, s2 op_sel_hi:[1,0]
	s_nop 0
	v_exp_f16_e32 v120, v2
	v_exp_f16_e32 v115, v3
	v_exp_f16_sdwa v120, v2 dst_sel:WORD_1 dst_unused:UNUSED_PRESERVE src0_sel:WORD_1
	v_exp_f16_sdwa v115, v3 dst_sel:WORD_1 dst_unused:UNUSED_PRESERVE src0_sel:WORD_1
	v_cvt_pk_f16_f32 v2, v14, v15
	v_cvt_pk_f16_f32 v3, v16, v17
	v_pk_max_i16 v2, v2, s2 op_sel_hi:[1,0]
	v_pk_max_i16 v3, v3, s2 op_sel_hi:[1,0]
	s_nop 0
	v_exp_f16_e32 v122, v2
	v_exp_f16_e32 v116, v3
	v_exp_f16_sdwa v122, v2 dst_sel:WORD_1 dst_unused:UNUSED_PRESERVE src0_sel:WORD_1
	v_exp_f16_sdwa v116, v3 dst_sel:WORD_1 dst_unused:UNUSED_PRESERVE src0_sel:WORD_1
	v_mfma_f32_32x32x16_bf16 v[2:17], v[18:21], v[124:127], 0
	s_nop 11
	v_cvt_pk_f16_f32 v2, v2, v3
	v_cvt_pk_f16_f32 v3, v4, v5
	v_pk_max_i16 v2, v2, s2 op_sel_hi:[1,0]
	v_pk_max_i16 v3, v3, s2 op_sel_hi:[1,0]
	s_nop 0
	v_exp_f16_e32 v124, v2
	v_exp_f16_e32 v119, v3
	v_exp_f16_sdwa v124, v2 dst_sel:WORD_1 dst_unused:UNUSED_PRESERVE src0_sel:WORD_1
	v_exp_f16_sdwa v119, v3 dst_sel:WORD_1 dst_unused:UNUSED_PRESERVE src0_sel:WORD_1
	v_cvt_pk_f16_f32 v2, v6, v7
	v_cvt_pk_f16_f32 v3, v8, v9
	v_pk_max_i16 v2, v2, s2 op_sel_hi:[1,0]
	v_pk_max_i16 v3, v3, s2 op_sel_hi:[1,0]
	s_nop 0
	v_exp_f16_e32 v125, v2
	v_exp_f16_e32 v121, v3
	v_exp_f16_sdwa v125, v2 dst_sel:WORD_1 dst_unused:UNUSED_PRESERVE src0_sel:WORD_1
	v_exp_f16_sdwa v121, v3 dst_sel:WORD_1 dst_unused:UNUSED_PRESERVE src0_sel:WORD_1
	v_cvt_pk_f16_f32 v2, v10, v11
	v_cvt_pk_f16_f32 v3, v12, v13
	v_pk_max_i16 v2, v2, s2 op_sel_hi:[1,0]
	v_pk_max_i16 v3, v3, s2 op_sel_hi:[1,0]
	s_nop 0
	v_exp_f16_e32 v126, v2
	v_exp_f16_e32 v123, v3
	v_exp_f16_sdwa v126, v2 dst_sel:WORD_1 dst_unused:UNUSED_PRESERVE src0_sel:WORD_1
	v_exp_f16_sdwa v123, v3 dst_sel:WORD_1 dst_unused:UNUSED_PRESERVE src0_sel:WORD_1
	v_cvt_pk_f16_f32 v2, v14, v15
	v_cvt_pk_f16_f32 v3, v16, v17
	v_pk_max_i16 v2, v2, s2 op_sel_hi:[1,0]
	v_pk_max_i16 v3, v3, s2 op_sel_hi:[1,0]
	s_nop 0
	v_exp_f16_e32 v127, v2
	v_exp_f16_e32 v17, v3
	v_exp_f16_sdwa v127, v2 dst_sel:WORD_1 dst_unused:UNUSED_PRESERVE src0_sel:WORD_1
	v_exp_f16_sdwa v17, v3 dst_sel:WORD_1 dst_unused:UNUSED_PRESERVE src0_sel:WORD_1
	s_branch .LBB3_39
.Lffc_touch_39:
	s_branch .Lffc_touch_ret
.LBB3_39:
	s_waitcnt vmcnt(5)
	v_rcp_f32_e32 v2, v133
	s_waitcnt vmcnt(4)
	v_rcp_f32_e32 v3, v132
	s_waitcnt vmcnt(3)
	v_rcp_f32_e32 v4, v131
	v_cmp_lt_f32_e32 vcc, 0, v133
	s_waitcnt vmcnt(2)
	v_rcp_f32_e32 v5, v130
	s_waitcnt vmcnt(1)
	v_rcp_f32_e32 v6, v129
	v_cndmask_b32_e32 v2, 0, v2, vcc
	v_cmp_lt_f32_e32 vcc, 0, v132
	s_waitcnt vmcnt(0)
	v_rcp_f32_e32 v7, v128
	s_getpc_b64 s[36:37]

_Z6k_iterILb0ELb1EEvPKfS1_PKiPK15HIP_vector_typeIfLj4EES7_S1_S1_S3_S1_PfS8_S1_S3_PDF16_PS5_SA_PiSA_SB_:
	s_and_b32 s38, s0, 0xfffff000
	s_mov_b32 s39, s1
	s_load_dwordx2 s[8:9], s[0:1], 0x80
	s_load_dwordx4 s[4:7], s[0:1], 0x70
	s_load_dwordx4 s[16:19], s[0:1], 0x40
	s_load_dwordx2 s[40:41], s[0:1], 0x90
	s_load_dwordx2 s[22:23], s[0:1], 0x50
	s_load_dwordx2 s[42:43], s[0:1], 0x88
	v_readfirstlane_b32 s12, v0
	v_cmp_gt_u32_e64 s[14:15], 64, v0
	v_lshlrev_b32_e32 v1, 2, v0
	s_and_saveexec_b64 s[10:11], s[14:15]
	v_mov_b32_e32 v2, 0
	ds_write_b32 v1, v2 offset:5152
	s_or_b64 exec, exec, s[10:11]
	s_lshl_b32 s3, s2, 5
	s_and_b32 s3, s3, 0xe0
	s_lshr_b32 s2, s2, 3
	s_add_i32 s2, s3, s2
	s_lshl_b32 s29, s2, 6
	v_and_b32_e32 v2, 31, v0
	v_or_b32_e32 v4, s29, v2
	v_mov_b32_e32 v5, 0
	s_lshr_b32 s30, s12, 6
	s_lshl_b32 s32, s30, 2
	s_lshr_b32 s32, 0x73261540, s32
	s_lshl_b32 s32, s32, 5
	s_and_b32 s32, s32, 0xe0
	v_or_b32_e32 v176, s32, v2
	v_lshlrev_b32_e32 v177, 4, v176
	v_add_u32_e32 v178, 0x1000, v177
	v_add_u32_e32 v179, 0x2000, v177
	v_add_u32_e32 v180, 0x3000, v177
	v_add_u32_e32 v181, 0x4000, v177
	v_add_u32_e32 v182, 0x5000, v177
	s_mov_b32 s3, 0
	s_lshl_b64 s[34:35], s[2:3], 16
	s_lshl_b32 s33, s2, 2
	s_waitcnt lgkmcnt(0)
	s_load_dword s26, s[8:9], s33 offset:0x0
	s_load_dword s41, s[40:41], s33 offset:0x0
	s_add_u32 s20, s4, s34
	s_addc_u32 s21, s5, s35
	v_lshl_add_u64 v[4:5], v[4:5], 4, s[6:7]
	global_load_dwordx3 v[30:32], v[4:5], off
	global_load_dwordx3 v[26:28], v[4:5], off offset:512
	global_load_dwordx4 v[2:5], v177, s[20:21]
	global_load_dwordx4 v[6:9], v178, s[20:21]
	global_load_dwordx4 v[10:13], v179, s[20:21]
	global_load_dwordx4 v[14:17], v180, s[20:21]
	global_load_dwordx4 v[18:21], v181, s[20:21]
	global_load_dwordx4 v[22:25], v182, s[20:21]
	s_cmp_eq_u32 s30, 0
	s_cbranch_scc1 .Lftc_touch_14
	s_cmp_eq_u32 s30, 1
	s_cbranch_scc1 .Lftc_touch_19
	s_cmp_eq_u32 s30, 2
	s_cbranch_scc1 .Lftc_touch_11
	s_cmp_eq_u32 s30, 3
	s_cbranch_scc1 .Lftc_touch_15
	s_cmp_eq_u32 s30, 4
	s_cbranch_scc1 .Lftc_touch_31
	s_cmp_eq_u32 s30, 5
	s_cbranch_scc1 .Lftc_touch_37
	s_cmp_eq_u32 s30, 6
	s_cbranch_scc1 .Lftc_touch_39
.Lftc_touch_ret:
	v_and_b32_e32 v38, 63, v0
	v_mov_b32_e32 v29, 0xff800000
	v_cmp_gt_u32_e64 s[0:1], 32, v38
	s_waitcnt lgkmcnt(0)
	s_cmpk_gt_i32 s26, 0x600
	s_cselect_b64 s[24:25], -1, 0
	s_cmpk_lt_i32 s26, 0x601
	s_cbranch_scc1 .LBB4_6
	s_and_saveexec_b64 s[8:9], s[14:15]
	s_cbranch_execz .LBB4_5
	v_or_b32_e32 v178, s29, v0
	v_mov_b32_e32 v179, 0
	v_lshl_add_u64 v[178:179], v[178:179], 4, s[6:7]
	global_load_dwordx4 v[178:181], v[178:179], off
	v_lshlrev_b32_e32 v177, 4, v0
	s_waitcnt vmcnt(0)
	ds_write_b128 v177, v[178:181] offset:2080

.Lftc_nocache1:
	s_cmp_lt_i32 s28, 4
	global_load_dword v133, v[6:7], off
	global_load_dword v132, v[8:9], off
	global_load_dword v131, v[10:11], off
	global_load_dword v130, v[12:13], off
	global_load_dword v129, v[14:15], off
	global_load_dword v128, v[4:5], off
	v_max_f32_e32 v6, v32, v32
	v_cndmask_b32_e64 v4, v31, v30, s[0:1]
	v_max_f32_e32 v6, 0xc6ea6000, v6
	v_cndmask_b32_e64 v6, v6, 1.0, s[0:1]
	v_and_b32_e32 v7, 0xffff0000, v4
	v_sub_f32_e32 v8, v4, v7
	v_or_b32_sdwa v22, v4, v7 dst_sel:DWORD dst_unused:UNUSED_PAD src0_sel:WORD_1 src1_sel:DWORD
	v_and_b32_e32 v4, 0xffff0000, v6
	v_sub_f32_e32 v7, v6, v4
	v_or_b32_sdwa v24, v6, v4 dst_sel:DWORD dst_unused:UNUSED_PAD src0_sel:WORD_1 src1_sel:DWORD
	v_or_b32_sdwa v23, v8, v4 dst_sel:DWORD dst_unused:UNUSED_PAD src0_sel:WORD_1 src1_sel:DWORD
	v_max_f32_e32 v4, v28, v28
	v_cndmask_b32_e64 v5, v27, v26, s[0:1]
	v_and_b32_e32 v9, 0xffff0000, v7
	v_max_f32_e32 v4, 0xc6ea6000, v4
	v_sub_f32_e32 v9, v7, v9
	v_lshrrev_b32_e32 v7, 16, v7
	v_cndmask_b32_e64 v4, v4, 1.0, s[0:1]
	v_and_b32_e32 v6, 0xffff0000, v5
	v_and_or_b32 v25, v9, s2, v7
	v_sub_f32_e32 v7, v5, v6
	v_or_b32_sdwa v18, v5, v6 dst_sel:DWORD dst_unused:UNUSED_PAD src0_sel:WORD_1 src1_sel:DWORD
	v_and_b32_e32 v5, 0xffff0000, v4
	v_sub_f32_e32 v6, v4, v5
	v_and_b32_e32 v8, 0xffff0000, v6
	v_sub_f32_e32 v8, v6, v8
	v_lshrrev_b32_e32 v6, 16, v6
	v_or_b32_sdwa v20, v4, v5 dst_sel:DWORD dst_unused:UNUSED_PAD src0_sel:WORD_1 src1_sel:DWORD
	v_or_b32_sdwa v19, v7, v5 dst_sel:DWORD dst_unused:UNUSED_PAD src0_sel:WORD_1 src1_sel:DWORD
	v_and_or_b32 v21, v8, s2, v6
	s_mov_b64 s[2:3], 0
	s_cbranch_scc1 .LBB4_11
	s_cmp_gt_i32 s28, 4
	s_cbranch_scc0 .LBB4_14
	s_cmp_gt_i32 s28, 5
	s_cbranch_scc0 .LBB4_15
	s_cmp_eq_u32 s28, 6
	s_mov_b64 s[4:5], 0
	s_cbranch_scc0 .LBB4_48
	v_and_b32_e32 v4, 0xffff0000, v2
	v_max_f32_e32 v3, v3, v3
	v_sub_f32_e32 v4, v2, v4
	v_max_f32_e32 v3, 0xc6ea6000, v3
	v_and_b32_e32 v5, 0xffff0000, v3
	v_and_b32_e32 v4, 0xffff0000, v4
	v_or_b32_sdwa v75, v5, v2 dst_sel:DWORD dst_unused:UNUSED_PAD src0_sel:DWORD src1_sel:WORD_1
	v_or_b32_sdwa v74, v4, v2 dst_sel:DWORD dst_unused:UNUSED_PAD src0_sel:DWORD src1_sel:WORD_1
	v_sub_f32_e32 v2, v3, v5
	v_and_b32_e32 v4, 0xffff0000, v2
	s_mov_b32 s6, 0xffff0000
	v_sub_f32_e32 v4, v2, v4
	v_lshrrev_b32_e32 v2, 16, v2
	v_and_or_b32 v76, v4, s6, v2
	v_or_b32_sdwa v77, v3, v5 dst_sel:DWORD dst_unused:UNUSED_PAD src0_sel:WORD_1 src1_sel:DWORD
	s_movk_i32 s6, 0xfc00
	s_mov_b64 s[8:9], -1
	v_mfma_f32_32x32x16_bf16 v[2:17], v[22:25], v[74:77], 0
	s_nop 11
	v_cvt_pk_f16_f32 v2, v2, v3
	v_cvt_pk_f16_f32 v3, v4, v5
	v_pk_max_i16 v2, v2, s6 op_sel_hi:[1,0]
	v_pk_max_i16 v3, v3, s6 op_sel_hi:[1,0]
	s_nop 0
	v_exp_f16_e32 v43, v2
	v_exp_f16_e32 v45, v3
	v_exp_f16_sdwa v43, v2 dst_sel:WORD_1 dst_unused:UNUSED_PRESERVE src0_sel:WORD_1
	v_exp_f16_sdwa v45, v3 dst_sel:WORD_1 dst_unused:UNUSED_PRESERVE src0_sel:WORD_1
	v_cvt_pk_f16_f32 v2, v6, v7
	v_cvt_pk_f16_f32 v3, v8, v9
	v_pk_max_i16 v2, v2, s6 op_sel_hi:[1,0]
	v_pk_max_i16 v3, v3, s6 op_sel_hi:[1,0]
	s_nop 0
	v_exp_f16_e32 v50, v2
	v_exp_f16_e32 v54, v3
	v_exp_f16_sdwa v50, v2 dst_sel:WORD_1 dst_unused:UNUSED_PRESERVE src0_sel:WORD_1
	v_exp_f16_sdwa v54, v3 dst_sel:WORD_1 dst_unused:UNUSED_PRESERVE src0_sel:WORD_1
	v_cvt_pk_f16_f32 v2, v10, v11
	v_cvt_pk_f16_f32 v3, v12, v13
	v_pk_max_i16 v2, v2, s6 op_sel_hi:[1,0]
	v_pk_max_i16 v3, v3, s6 op_sel_hi:[1,0]
	s_nop 0
	v_exp_f16_e32 v58, v2
	v_exp_f16_e32 v61, v3
	v_exp_f16_sdwa v58, v2 dst_sel:WORD_1 dst_unused:UNUSED_PRESERVE src0_sel:WORD_1
	v_exp_f16_sdwa v61, v3 dst_sel:WORD_1 dst_unused:UNUSED_PRESERVE src0_sel:WORD_1
	v_cvt_pk_f16_f32 v2, v14, v15
	v_cvt_pk_f16_f32 v3, v16, v17
	v_pk_max_i16 v2, v2, s6 op_sel_hi:[1,0]
	v_pk_max_i16 v3, v3, s6 op_sel_hi:[1,0]
	s_nop 0
	v_exp_f16_e32 v64, v2
	v_exp_f16_e32 v66, v3
	v_exp_f16_sdwa v64, v2 dst_sel:WORD_1 dst_unused:UNUSED_PRESERVE src0_sel:WORD_1
	v_exp_f16_sdwa v66, v3 dst_sel:WORD_1 dst_unused:UNUSED_PRESERVE src0_sel:WORD_1
	v_mfma_f32_32x32x16_bf16 v[2:17], v[18:21], v[74:77], 0
	s_nop 11
	v_cvt_pk_f16_f32 v2, v2, v3
	v_cvt_pk_f16_f32 v3, v4, v5
	v_pk_max_i16 v2, v2, s6 op_sel_hi:[1,0]
	v_pk_max_i16 v3, v3, s6 op_sel_hi:[1,0]
	s_nop 0
	v_exp_f16_e32 v72, v2
	v_exp_f16_e32 v76, v3
	v_exp_f16_sdwa v72, v2 dst_sel:WORD_1 dst_unused:UNUSED_PRESERVE src0_sel:WORD_1
	v_exp_f16_sdwa v76, v3 dst_sel:WORD_1 dst_unused:UNUSED_PRESERVE src0_sel:WORD_1
	v_cvt_pk_f16_f32 v2, v6, v7
	v_cvt_pk_f16_f32 v3, v8, v9
	v_pk_max_i16 v2, v2, s6 op_sel_hi:[1,0]
	v_pk_max_i16 v3, v3, s6 op_sel_hi:[1,0]
	s_nop 0
	v_exp_f16_e32 v83, v2
	v_exp_f16_e32 v85, v3
	v_exp_f16_sdwa v83, v2 dst_sel:WORD_1 dst_unused:UNUSED_PRESERVE src0_sel:WORD_1
	v_exp_f16_sdwa v85, v3 dst_sel:WORD_1 dst_unused:UNUSED_PRESERVE src0_sel:WORD_1
	v_cvt_pk_f16_f32 v2, v10, v11
	v_cvt_pk_f16_f32 v3, v12, v13
	v_pk_max_i16 v2, v2, s6 op_sel_hi:[1,0]
	v_pk_max_i16 v3, v3, s6 op_sel_hi:[1,0]
	s_nop 0
	v_exp_f16_e32 v89, v2
	v_exp_f16_e32 v92, v3
	v_exp_f16_sdwa v89, v2 dst_sel:WORD_1 dst_unused:UNUSED_PRESERVE src0_sel:WORD_1
	v_exp_f16_sdwa v92, v3 dst_sel:WORD_1 dst_unused:UNUSED_PRESERVE src0_sel:WORD_1
	v_cvt_pk_f16_f32 v2, v14, v15
	v_cvt_pk_f16_f32 v3, v16, v17
	v_pk_max_i16 v2, v2, s6 op_sel_hi:[1,0]
	v_pk_max_i16 v3, v3, s6 op_sel_hi:[1,0]
	s_nop 0
	v_exp_f16_e32 v95, v2
	v_exp_f16_e32 v96, v3
	v_exp_f16_sdwa v95, v2 dst_sel:WORD_1 dst_unused:UNUSED_PRESERVE src0_sel:WORD_1
	v_exp_f16_sdwa v96, v3 dst_sel:WORD_1 dst_unused:UNUSED_PRESERVE src0_sel:WORD_1
	s_and_b64 vcc, exec, s[4:5]
	s_cbranch_vccnz .LBB4_16
	s_branch .LBB4_17
.Lftc_touch_11:
	s_branch .Lftc_touch_ret
.LBB4_11:
	s_mov_b64 s[4:5], 0
	s_cbranch_execnz .LBB4_24

.LBB4_13:
	v_max_f32_e32 v2, v70, v70
	v_max_f32_e32 v2, 0xc6ea6000, v2
	v_and_b32_e32 v4, 0xffff0000, v2
	v_and_b32_e32 v3, 0xffff0000, v68
	v_sub_f32_e32 v5, v2, v4
	v_sub_f32_e32 v3, v68, v3
	v_and_b32_e32 v6, 0xffff0000, v5
	s_mov_b32 s4, 0xffff0000
	v_and_b32_e32 v3, 0xffff0000, v3
	v_sub_f32_e32 v6, v5, v6
	v_lshrrev_b32_e32 v5, 16, v5
	v_or_b32_sdwa v101, v4, v68 dst_sel:DWORD dst_unused:UNUSED_PAD src0_sel:DWORD src1_sel:WORD_1
	v_or_b32_sdwa v100, v3, v68 dst_sel:DWORD dst_unused:UNUSED_PAD src0_sel:DWORD src1_sel:WORD_1
	v_and_or_b32 v102, v6, s4, v5
	v_or_b32_sdwa v103, v2, v4 dst_sel:DWORD dst_unused:UNUSED_PAD src0_sel:WORD_1 src1_sel:DWORD
	s_movk_i32 s4, 0xfc00
	s_nop 0
	v_mfma_f32_32x32x16_bf16 v[2:17], v[22:25], v[100:103], 0
	s_nop 11
	v_cvt_pk_f16_f32 v2, v2, v3
	v_cvt_pk_f16_f32 v3, v4, v5
	v_pk_max_i16 v2, v2, s4 op_sel_hi:[1,0]
	v_pk_max_i16 v3, v3, s4 op_sel_hi:[1,0]
	s_nop 0
	v_exp_f16_e32 v68, v2
	v_exp_f16_e32 v70, v3
	v_exp_f16_sdwa v68, v2 dst_sel:WORD_1 dst_unused:UNUSED_PRESERVE src0_sel:WORD_1
	v_exp_f16_sdwa v70, v3 dst_sel:WORD_1 dst_unused:UNUSED_PRESERVE src0_sel:WORD_1
	v_cvt_pk_f16_f32 v2, v6, v7
	v_cvt_pk_f16_f32 v3, v8, v9
	v_pk_max_i16 v2, v2, s4 op_sel_hi:[1,0]
	v_pk_max_i16 v3, v3, s4 op_sel_hi:[1,0]
	s_nop 0
	v_exp_f16_e32 v71, v2
	v_exp_f16_e32 v73, v3
	v_exp_f16_sdwa v71, v2 dst_sel:WORD_1 dst_unused:UNUSED_PRESERVE src0_sel:WORD_1
	v_exp_f16_sdwa v73, v3 dst_sel:WORD_1 dst_unused:UNUSED_PRESERVE src0_sel:WORD_1
	v_cvt_pk_f16_f32 v2, v10, v11
	v_cvt_pk_f16_f32 v3, v12, v13
	v_pk_max_i16 v2, v2, s4 op_sel_hi:[1,0]
	v_pk_max_i16 v3, v3, s4 op_sel_hi:[1,0]
	s_nop 0
	v_exp_f16_e32 v77, v2
	v_exp_f16_e32 v78, v3
	v_exp_f16_sdwa v77, v2 dst_sel:WORD_1 dst_unused:UNUSED_PRESERVE src0_sel:WORD_1
	v_exp_f16_sdwa v78, v3 dst_sel:WORD_1 dst_unused:UNUSED_PRESERVE src0_sel:WORD_1
	v_cvt_pk_f16_f32 v2, v14, v15
	v_cvt_pk_f16_f32 v3, v16, v17
	v_pk_max_i16 v2, v2, s4 op_sel_hi:[1,0]
	v_pk_max_i16 v3, v3, s4 op_sel_hi:[1,0]
	s_nop 0
	v_exp_f16_e32 v81, v2
	v_exp_f16_e32 v82, v3
	v_exp_f16_sdwa v81, v2 dst_sel:WORD_1 dst_unused:UNUSED_PRESERVE src0_sel:WORD_1
	v_exp_f16_sdwa v82, v3 dst_sel:WORD_1 dst_unused:UNUSED_PRESERVE src0_sel:WORD_1
	v_mfma_f32_32x32x16_bf16 v[2:17], v[18:21], v[100:103], 0
	s_nop 11
	v_cvt_pk_f16_f32 v2, v2, v3
	v_cvt_pk_f16_f32 v3, v4, v5
	v_pk_max_i16 v2, v2, s4 op_sel_hi:[1,0]
	v_pk_max_i16 v3, v3, s4 op_sel_hi:[1,0]
	s_nop 0
	v_exp_f16_e32 v84, v2
	v_exp_f16_e32 v86, v3
	v_exp_f16_sdwa v84, v2 dst_sel:WORD_1 dst_unused:UNUSED_PRESERVE src0_sel:WORD_1
	v_exp_f16_sdwa v86, v3 dst_sel:WORD_1 dst_unused:UNUSED_PRESERVE src0_sel:WORD_1
	v_cvt_pk_f16_f32 v2, v6, v7
	v_cvt_pk_f16_f32 v3, v8, v9
	v_pk_max_i16 v2, v2, s4 op_sel_hi:[1,0]
	v_pk_max_i16 v3, v3, s4 op_sel_hi:[1,0]
	s_nop 0
	v_exp_f16_e32 v87, v2
	v_exp_f16_e32 v88, v3
	v_exp_f16_sdwa v87, v2 dst_sel:WORD_1 dst_unused:UNUSED_PRESERVE src0_sel:WORD_1
	v_exp_f16_sdwa v88, v3 dst_sel:WORD_1 dst_unused:UNUSED_PRESERVE src0_sel:WORD_1
	v_cvt_pk_f16_f32 v2, v10, v11
	v_cvt_pk_f16_f32 v3, v12, v13
	v_pk_max_i16 v2, v2, s4 op_sel_hi:[1,0]
	v_pk_max_i16 v3, v3, s4 op_sel_hi:[1,0]
	s_nop 0
	v_exp_f16_e32 v90, v2
	v_exp_f16_e32 v91, v3
	v_exp_f16_sdwa v90, v2 dst_sel:WORD_1 dst_unused:UNUSED_PRESERVE src0_sel:WORD_1
	v_exp_f16_sdwa v91, v3 dst_sel:WORD_1 dst_unused:UNUSED_PRESERVE src0_sel:WORD_1
	v_cvt_pk_f16_f32 v2, v14, v15
	v_cvt_pk_f16_f32 v3, v16, v17
	v_pk_max_i16 v2, v2, s4 op_sel_hi:[1,0]
	v_pk_max_i16 v3, v3, s4 op_sel_hi:[1,0]
	s_mov_b64 s[4:5], -1
	v_exp_f16_e32 v93, v2
	v_exp_f16_e32 v94, v3
	v_exp_f16_sdwa v93, v2 dst_sel:WORD_1 dst_unused:UNUSED_PRESERVE src0_sel:WORD_1
	v_exp_f16_sdwa v94, v3 dst_sel:WORD_1 dst_unused:UNUSED_PRESERVE src0_sel:WORD_1
	s_andn2_b64 vcc, exec, s[6:7]
	s_cbranch_vccz .LBB4_30
	s_branch .LBB4_31
.Lftc_touch_14:
	s_branch .Lftc_touch_ret
.LBB4_14:
	s_mov_b64 s[4:5], 0
	s_cbranch_execz .LBB4_21
	s_branch .LBB4_20
.Lftc_touch_15:
	s_branch .Lftc_touch_ret
.LBB4_15:
	s_mov_b64 s[8:9], 0
	s_cbranch_execz .LBB4_17

.LBB4_17:
	s_mov_b64 s[6:7], 0
	s_andn2_b64 vcc, exec, s[8:9]
	s_mov_b64 s[4:5], 0
	s_cbranch_vccnz .LBB4_19
	v_max_f32_e32 v2, v48, v48
	v_max_f32_e32 v2, 0xc6ea6000, v2
	v_and_b32_e32 v4, 0xffff0000, v2
	v_and_b32_e32 v3, 0xffff0000, v46
	v_sub_f32_e32 v5, v2, v4
	v_sub_f32_e32 v3, v46, v3
	v_and_b32_e32 v6, 0xffff0000, v5
	s_mov_b32 s4, 0xffff0000
	v_and_b32_e32 v3, 0xffff0000, v3
	v_sub_f32_e32 v6, v5, v6
	v_lshrrev_b32_e32 v5, 16, v5
	v_or_b32_sdwa v47, v4, v46 dst_sel:DWORD dst_unused:UNUSED_PAD src0_sel:DWORD src1_sel:WORD_1
	v_or_b32_sdwa v46, v3, v46 dst_sel:DWORD dst_unused:UNUSED_PAD src0_sel:DWORD src1_sel:WORD_1
	v_and_or_b32 v48, v6, s4, v5
	v_or_b32_sdwa v49, v2, v4 dst_sel:DWORD dst_unused:UNUSED_PAD src0_sel:WORD_1 src1_sel:DWORD
	s_movk_i32 s4, 0xfc00
	s_nop 0
	v_mfma_f32_32x32x16_bf16 v[2:17], v[22:25], v[46:49], 0
	s_nop 11
	v_cvt_pk_f16_f32 v2, v2, v3
	v_cvt_pk_f16_f32 v3, v4, v5
	v_pk_max_i16 v2, v2, s4 op_sel_hi:[1,0]
	v_pk_max_i16 v3, v3, s4 op_sel_hi:[1,0]
	s_nop 0
	v_exp_f16_e32 v26, v2
	v_exp_f16_e32 v27, v3
	v_exp_f16_sdwa v26, v2 dst_sel:WORD_1 dst_unused:UNUSED_PRESERVE src0_sel:WORD_1
	v_exp_f16_sdwa v27, v3 dst_sel:WORD_1 dst_unused:UNUSED_PRESERVE src0_sel:WORD_1
	v_cvt_pk_f16_f32 v2, v6, v7
	v_cvt_pk_f16_f32 v3, v8, v9
	v_pk_max_i16 v2, v2, s4 op_sel_hi:[1,0]
	v_pk_max_i16 v3, v3, s4 op_sel_hi:[1,0]
	s_nop 0
	v_exp_f16_e32 v28, v2
	v_exp_f16_e32 v30, v3
	v_exp_f16_sdwa v28, v2 dst_sel:WORD_1 dst_unused:UNUSED_PRESERVE src0_sel:WORD_1
	v_exp_f16_sdwa v30, v3 dst_sel:WORD_1 dst_unused:UNUSED_PRESERVE src0_sel:WORD_1
	v_cvt_pk_f16_f32 v2, v10, v11
	v_cvt_pk_f16_f32 v3, v12, v13
	v_pk_max_i16 v2, v2, s4 op_sel_hi:[1,0]
	v_pk_max_i16 v3, v3, s4 op_sel_hi:[1,0]
	s_nop 0
	v_exp_f16_e32 v31, v2
	v_exp_f16_e32 v32, v3
	v_exp_f16_sdwa v31, v2 dst_sel:WORD_1 dst_unused:UNUSED_PRESERVE src0_sel:WORD_1
	v_exp_f16_sdwa v32, v3 dst_sel:WORD_1 dst_unused:UNUSED_PRESERVE src0_sel:WORD_1
	v_cvt_pk_f16_f32 v2, v14, v15
	v_cvt_pk_f16_f32 v3, v16, v17
	v_pk_max_i16 v2, v2, s4 op_sel_hi:[1,0]
	v_pk_max_i16 v3, v3, s4 op_sel_hi:[1,0]
	s_nop 0
	v_exp_f16_e32 v39, v2
	v_exp_f16_e32 v40, v3
	v_exp_f16_sdwa v39, v2 dst_sel:WORD_1 dst_unused:UNUSED_PRESERVE src0_sel:WORD_1
	v_exp_f16_sdwa v40, v3 dst_sel:WORD_1 dst_unused:UNUSED_PRESERVE src0_sel:WORD_1
	v_mfma_f32_32x32x16_bf16 v[2:17], v[18:21], v[46:49], 0
	s_nop 11
	v_cvt_pk_f16_f32 v2, v2, v3
	v_cvt_pk_f16_f32 v3, v4, v5
	v_pk_max_i16 v2, v2, s4 op_sel_hi:[1,0]
	v_pk_max_i16 v3, v3, s4 op_sel_hi:[1,0]
	s_nop 0
	v_exp_f16_e32 v41, v2
	v_exp_f16_e32 v42, v3
	v_exp_f16_sdwa v41, v2 dst_sel:WORD_1 dst_unused:UNUSED_PRESERVE src0_sel:WORD_1
	v_exp_f16_sdwa v42, v3 dst_sel:WORD_1 dst_unused:UNUSED_PRESERVE src0_sel:WORD_1
	v_cvt_pk_f16_f32 v2, v6, v7
	v_cvt_pk_f16_f32 v3, v8, v9
	v_pk_max_i16 v2, v2, s4 op_sel_hi:[1,0]
	v_pk_max_i16 v3, v3, s4 op_sel_hi:[1,0]
	s_nop 0
	v_exp_f16_e32 v44, v2
	v_exp_f16_e32 v47, v3
	v_exp_f16_sdwa v44, v2 dst_sel:WORD_1 dst_unused:UNUSED_PRESERVE src0_sel:WORD_1
	v_exp_f16_sdwa v47, v3 dst_sel:WORD_1 dst_unused:UNUSED_PRESERVE src0_sel:WORD_1
	v_cvt_pk_f16_f32 v2, v10, v11
	v_cvt_pk_f16_f32 v3, v12, v13
	v_pk_max_i16 v2, v2, s4 op_sel_hi:[1,0]
	v_pk_max_i16 v3, v3, s4 op_sel_hi:[1,0]
	s_nop 0
	v_exp_f16_e32 v51, v2
	v_exp_f16_e32 v53, v3
	v_exp_f16_sdwa v51, v2 dst_sel:WORD_1 dst_unused:UNUSED_PRESERVE src0_sel:WORD_1
	v_exp_f16_sdwa v53, v3 dst_sel:WORD_1 dst_unused:UNUSED_PRESERVE src0_sel:WORD_1
	v_cvt_pk_f16_f32 v2, v14, v15
	v_cvt_pk_f16_f32 v3, v16, v17
	v_pk_max_i16 v2, v2, s4 op_sel_hi:[1,0]
	v_pk_max_i16 v3, v3, s4 op_sel_hi:[1,0]
	s_mov_b64 s[4:5], -1
	v_exp_f16_e32 v57, v2
	v_exp_f16_e32 v59, v3
	v_exp_f16_sdwa v57, v2 dst_sel:WORD_1 dst_unused:UNUSED_PRESERVE src0_sel:WORD_1
	v_exp_f16_sdwa v59, v3 dst_sel:WORD_1 dst_unused:UNUSED_PRESERVE src0_sel:WORD_1
	s_and_b64 vcc, exec, s[6:7]
	s_cbranch_vccz .LBB4_21
	s_branch .LBB4_20
.Lftc_touch_19:
	s_branch .Lftc_touch_ret
.LBB4_19:
	s_and_b64 vcc, exec, s[6:7]
	s_cbranch_vccz .LBB4_21

.LBB4_29:
	s_mov_b64 s[4:5], 0
	s_andn2_b64 vcc, exec, s[6:7]
	s_cbranch_vccnz .LBB4_31
.LBB4_30:
	s_mov_b64 s[4:5], -1
	s_branch .LBB4_31
.Lftc_touch_31:
	s_branch .Lftc_touch_ret
.LBB4_31:
	s_andn2_b64 vcc, exec, s[4:5]
	s_cbranch_vccnz .LBB4_33
	s_cmp_eq_u32 s36, 0
	s_cbranch_scc1 .Lftc_nb1_compute
	s_waitcnt vmcnt(6)
	v_mov_b32_e32 v98, v200
	v_mov_b32_e32 v97, v201
	v_mov_b32_e32 v100, v202
	v_mov_b32_e32 v99, v203
	v_mov_b32_e32 v102, v204
	v_mov_b32_e32 v101, v205
	v_mov_b32_e32 v104, v206
	v_mov_b32_e32 v103, v207
	v_mov_b32_e32 v106, v208
	v_mov_b32_e32 v105, v209
	v_mov_b32_e32 v108, v210
	v_mov_b32_e32 v107, v211
	v_mov_b32_e32 v110, v212
	v_mov_b32_e32 v109, v213
	v_mov_b32_e32 v112, v214
	v_mov_b32_e32 v111, v215
	s_mov_b64 s[4:5], -1
	s_andn2_b64 vcc, exec, s[2:3]
	s_cbranch_vccz .LBB4_34
	s_branch .LBB4_37

.LBB4_34:
	s_cmp_eq_u32 s28, 1
	s_cbranch_scc0 .LBB4_36
	s_mov_b64 s[4:5], -1
.LBB4_36:
	s_branch .LBB4_37
.Lftc_touch_37:
	s_branch .Lftc_touch_ret
.LBB4_37:
	s_and_b64 vcc, exec, s[4:5]
	s_cbranch_vccz .LBB4_39
	s_cmp_eq_u32 s47, 0
	s_cbranch_scc1 .Lftc_nb0_compute
	s_waitcnt vmcnt(6)
	v_mov_b32_e32 v117, v184
	v_mov_b32_e32 v113, v185
	v_mov_b32_e32 v118, v186
	v_mov_b32_e32 v114, v187
	v_mov_b32_e32 v120, v188
	v_mov_b32_e32 v115, v189
	v_mov_b32_e32 v122, v190
	v_mov_b32_e32 v116, v191
	v_mov_b32_e32 v124, v192
	v_mov_b32_e32 v119, v193
	v_mov_b32_e32 v125, v194
	v_mov_b32_e32 v121, v195
	v_mov_b32_e32 v126, v196
	v_mov_b32_e32 v123, v197
	v_mov_b32_e32 v127, v198
	v_mov_b32_e32 v17, v199
	s_branch .LBB4_39

.LBB4_39:
	s_waitcnt vmcnt(5)
	v_rcp_f32_e32 v2, v133
	s_waitcnt vmcnt(4)
	v_rcp_f32_e32 v3, v132
	s_waitcnt vmcnt(3)
	v_rcp_f32_e32 v4, v131
	v_cmp_lt_f32_e32 vcc, 0, v133
	s_waitcnt vmcnt(2)
	v_rcp_f32_e32 v5, v130
	s_waitcnt vmcnt(1)
	v_rcp_f32_e32 v6, v129
	v_cndmask_b32_e32 v2, 0, v2, vcc
	v_cmp_lt_f32_e32 vcc, 0, v132
	s_waitcnt vmcnt(0)
	v_rcp_f32_e32 v7, v128
	s_getpc_b64 s[36:37]
	s_sub_u32 s36, s36, 0x97f0
	s_subb_u32 s37, s37, 0
	v_lshlrev_b32_e32 v183, 6, v0
	v_min_u32_e32 v183, 0x1d80, v183
	global_load_dword v183, v183, s[36:37]
	v_lshlrev_b32_e32 v182, 6, v38
	global_load_dword v182, v182, s[38:39]
	s_lshl_b32 s40, s29, 10
	s_add_u32 s40, s42, s40
	s_addc_u32 s41, s43, 0
	v_lshlrev_b32_e32 v181, 6, v0
	v_and_b32_e32 v181, 0x7fc0, v181
	global_load_dword v181, v181, s[40:41]
	s_mov_b32 s4, 0x42c80000
	v_cndmask_b32_e32 v3, 0, v3, vcc
	v_cmp_lt_f32_e32 vcc, 0, v131
	v_cmp_ngt_f32_e64 s[2:3], s4, v3
	s_mov_b64 s[6:7], 0
	v_cndmask_b32_e32 v4, 0, v4, vcc
	v_cmp_lt_f32_e32 vcc, 0, v130
	s_nop 1
	v_cndmask_b32_e32 v5, 0, v5, vcc
	v_cmp_lt_f32_e32 vcc, 0, v129
	s_nop 1
	v_cndmask_b32_e32 v6, 0, v6, vcc
	v_cmp_lt_f32_e32 vcc, 0, v128
	s_nop 1
	v_cndmask_b32_e32 v7, 0, v7, vcc
	v_cmp_ngt_f32_e32 vcc, s4, v2
	s_or_b64 s[2:3], vcc, s[2:3]
	v_cmp_ngt_f32_e32 vcc, s4, v4
	s_or_b64 s[2:3], s[2:3], vcc
	v_cmp_ngt_f32_e32 vcc, s4, v5
	s_or_b64 s[2:3], s[2:3], vcc
	v_cmp_ngt_f32_e32 vcc, s4, v6
	s_or_b64 s[2:3], s[2:3], vcc
	v_cmp_ngt_f32_e32 vcc, s4, v7
	s_or_b64 s[2:3], s[2:3], vcc
	v_cndmask_b32_e64 v8, 0, 1, s[2:3]
	v_cmp_ne_u32_e32 vcc, 0, v8
	s_cmp_eq_u64 vcc, 0
	s_cselect_b64 s[2:3], -1, 0
	v_cndmask_b32_e64 v8, 0, 1, s[2:3]
	s_nop 0
	v_readfirstlane_b32 s2, v8
	s_bitcmp0_b32 s2, 0
	s_cbranch_scc0 .LBB4_45
	s_cmp_lt_i32 s28, 4
	s_cbranch_scc1 .LBB4_46
	s_cmp_gt_i32 s28, 4
	s_cbranch_scc0 .LBB4_47
	s_mov_b64 s[4:5], -1
	v_mov_b32_e32 v8, 0
	s_cmp_gt_i32 s28, 5
	v_mov_b32_e32 v167, 0
	v_mov_b32_e32 v166, 0
	v_mov_b32_e32 v165, 0
	v_mov_b32_e32 v164, 0
	v_mov_b32_e32 v162, 0
	v_mov_b32_e32 v160, 0
	v_mov_b32_e32 v159, 0
	v_mov_b32_e32 v157, 0
	v_mov_b32_e32 v151, 0
	v_mov_b32_e32 v149, 0
	v_mov_b32_e32 v147, 0
	v_mov_b32_e32 v146, 0
	v_mov_b32_e32 v144, 0
	v_mov_b32_e32 v143, 0
	v_mov_b32_e32 v152, 0
	v_mov_b32_e32 v153, 0
	v_mov_b32_e32 v154, 0
	v_mov_b32_e32 v155, 0
	v_mov_b32_e32 v156, 0
	v_mov_b32_e32 v158, 0
	v_mov_b32_e32 v161, 0
	v_mov_b32_e32 v163, 0
	v_mov_b32_e32 v168, 0
	v_mov_b32_e32 v169, 0
	v_mov_b32_e32 v170, 0
	v_mov_b32_e32 v171, 0
	v_mov_b32_e32 v172, 0
	v_mov_b32_e32 v173, 0
	v_mov_b32_e32 v174, 0
	v_mov_b32_e32 v145, 0
	v_mov_b32_e32 v148, 0
	v_mov_b32_e32 v150, 0
	s_cbranch_scc0 .LBB4_50
	s_cmp_eq_u32 s28, 6
	s_cbranch_scc0 .LBB4_49
	v_mov_b32_e32 v145, 0
	v_mov_b32_e32 v148, 0
	v_mov_b32_e32 v150, 0
	v_mov_b32_e32 v143, 0
	v_mov_b32_e32 v144, 0
	v_mov_b32_e32 v146, 0
	v_mov_b32_e32 v147, 0
	v_mov_b32_e32 v149, 0
	v_mov_b32_e32 v151, 0
	v_mov_b32_e32 v152, 0
	v_mov_b32_e32 v153, 0
	v_mov_b32_e32 v154, 0
	v_mov_b32_e32 v155, 0
	v_mov_b32_e32 v156, 0
	v_mov_b32_e32 v158, 0
	v_mov_b32_e32 v161, 0
	v_mov_b32_e32 v163, 0
	v_mov_b32_e32 v157, 0
	v_mov_b32_e32 v159, 0
	v_mov_b32_e32 v160, 0
	v_mov_b32_e32 v162, 0
	v_mov_b32_e32 v164, 0
	v_mov_b32_e32 v165, 0
	v_mov_b32_e32 v166, 0
	v_mov_b32_e32 v167, 0
	v_mov_b32_e32 v168, 0
	v_mov_b32_e32 v169, 0
	v_mov_b32_e32 v170, 0
	v_mov_b32_e32 v171, 0
	v_mov_b32_e32 v172, 0
	v_mov_b32_e32 v173, 0
	v_mov_b32_e32 v174, 0
	v_fma_mix_f32 v148, v43, v7, v148 op_sel_hi:[1,0,0]
	v_fma_mix_f32 v150, v45, v7, v150 op_sel_hi:[1,0,0]
	v_fma_mix_f32 v143, v50, v7, v143 op_sel_hi:[1,0,0]
	v_fma_mix_f32 v144, v54, v7, v144 op_sel_hi:[1,0,0]
	v_fma_mix_f32 v146, v58, v7, v146 op_sel_hi:[1,0,0]
	v_fma_mix_f32 v147, v61, v7, v147 op_sel_hi:[1,0,0]
	v_fma_mix_f32 v149, v64, v7, v149 op_sel_hi:[1,0,0]
	v_fma_mix_f32 v151, v66, v7, v151 op_sel_hi:[1,0,0]
	v_fma_mix_f32 v152, v43, v7, v152 op_sel:[1,0,0] op_sel_hi:[1,0,0]
	v_fma_mix_f32 v153, v45, v7, v153 op_sel:[1,0,0] op_sel_hi:[1,0,0]
	v_fma_mix_f32 v154, v50, v7, v154 op_sel:[1,0,0] op_sel_hi:[1,0,0]
	v_fma_mix_f32 v155, v54, v7, v155 op_sel:[1,0,0] op_sel_hi:[1,0,0]
	v_fma_mix_f32 v156, v58, v7, v156 op_sel:[1,0,0] op_sel_hi:[1,0,0]
	v_fma_mix_f32 v158, v61, v7, v158 op_sel:[1,0,0] op_sel_hi:[1,0,0]
	v_fma_mix_f32 v161, v64, v7, v161 op_sel:[1,0,0] op_sel_hi:[1,0,0]
	v_fma_mix_f32 v163, v66, v7, v163 op_sel:[1,0,0] op_sel_hi:[1,0,0]
	v_fma_mix_f32 v157, v72, v7, v157 op_sel_hi:[1,0,0]
	v_fma_mix_f32 v159, v76, v7, v159 op_sel_hi:[1,0,0]
	v_fma_mix_f32 v160, v83, v7, v160 op_sel_hi:[1,0,0]
	v_fma_mix_f32 v162, v85, v7, v162 op_sel_hi:[1,0,0]
	v_fma_mix_f32 v164, v89, v7, v164 op_sel_hi:[1,0,0]
	v_fma_mix_f32 v165, v92, v7, v165 op_sel_hi:[1,0,0]
	v_fma_mix_f32 v166, v95, v7, v166 op_sel_hi:[1,0,0]
	v_fma_mix_f32 v167, v96, v7, v167 op_sel_hi:[1,0,0]
	v_fma_mix_f32 v168, v72, v7, v168 op_sel:[1,0,0] op_sel_hi:[1,0,0]
	v_fma_mix_f32 v169, v76, v7, v169 op_sel:[1,0,0] op_sel_hi:[1,0,0]
	v_fma_mix_f32 v170, v83, v7, v170 op_sel:[1,0,0] op_sel_hi:[1,0,0]
	v_fma_mix_f32 v171, v85, v7, v171 op_sel:[1,0,0] op_sel_hi:[1,0,0]
	v_fma_mix_f32 v172, v89, v7, v172 op_sel:[1,0,0] op_sel_hi:[1,0,0]
	v_fma_mix_f32 v173, v92, v7, v173 op_sel:[1,0,0] op_sel_hi:[1,0,0]
	v_fma_mix_f32 v174, v95, v7, v174 op_sel:[1,0,0] op_sel_hi:[1,0,0]
	v_fma_mix_f32 v145, v96, v7, v145 op_sel:[1,0,0] op_sel_hi:[1,0,0]
	s_branch .LBB4_50
